# helper share raised to 5x171 runs (computing workgroups convert more of the tail)
# baseline (speedup 1.0000x reference)
; #define LDS_AS __attribute__((address_space(3)))
; #define OPAQUE_TID(P) (((P).wid0 << 6) | lane_id_now())
; template <int NS, bool STREAM_ONLY = false>
; DI void convert_experts_dma(const Params& p, LDS_AS unsigned char* lds, int bid, int nb) {
;   const int tid = OPAQUE_TID(p), wid = __builtin_amdgcn_readfirstlane(tid >> 6), lane = tid & 63;
;   constexpr int NT = 32 * 1536;
;   const int nvalid = bid < NT / CVG ? CVG * ((NT / CVG - bid + nb - 1) / nb) : 0;
; __global__ void __launch_bounds__(NTHREADS, 2) k_forward(Params p_in) {
;     ...
;     if (ncv == 0) convert_experts_dma<4>(p, lds, bid, nb);
.LBB0_1119:
	s_or_b64 exec, exec, s[0:1]
	s_mov_b64 s[12:13], 0
	s_mov_b32 s20, 0
	s_mov_b64 s[0:1], 0
	v_readlane_b32 s97, v255, 13
	s_mov_b32 s99, s96
	s_nop 0
	s_mov_b32 s98, s97
	s_cmp_lg_u32 s55, 0
	s_cbranch_scc0 .LBB0_1181
	v_readlane_b32 s98, v255, 17
	s_sub_i32 s99, s96, s55
	s_add_i32 s98, s98, 0x2ca9
	s_branch .LBB0_1181
.LBB0_1121:
	v_mov_b32_e32 v0, 0
	ds_read_b32 v2, v0
	ds_read_b32 v3, v0 offset:4
	s_waitcnt lgkmcnt(0)
	s_barrier
	v_mbcnt_lo_u32_b32 v0, -1, 0
	v_mbcnt_hi_u32_b32 v0, -1, v0
	s_mov_b32 s6, 0
	v_or_b32_e32 v1, s87, v0
	s_cmpk_gt_i32 s54, 0x2ca8
	v_readfirstlane_b32 s0, v1
	s_mov_b32 s18, 0
	s_cbranch_scc1 .LBB0_1123
	s_abs_i32 s1, s55
	v_cvt_f32_u32_e32 v1, s1
	s_sub_i32 s2, s55, s54
	s_add_i32 s3, s2, 0x2ca8
	s_sub_i32 s2, 0xffffd358, s2
	v_rcp_iflag_f32_e32 v1, v1
	s_xor_b32 s5, s3, s55
	s_sub_i32 s4, 0, s1
	s_max_i32 s2, s3, s2
	v_mul_f32_e32 v1, 0x4f7ffffe, v1
	v_cvt_u32_f32_e32 v1, v1
	s_ashr_i32 s3, s5, 31
	v_readfirstlane_b32 s5, v1
	s_mul_i32 s4, s4, s5
	s_mul_hi_u32 s4, s5, s4
	s_add_i32 s5, s5, s4
	s_mul_hi_u32 s4, s2, s5
	s_mul_i32 s5, s4, s1
	s_sub_i32 s2, s2, s5
	s_add_i32 s7, s4, 1
	s_sub_i32 s5, s2, s1
	s_cmp_ge_u32 s2, s1
	s_cselect_b32 s4, s7, s4
	s_cselect_b32 s2, s5, s2
	s_add_i32 s5, s4, 1
	s_cmp_ge_u32 s2, s1
	s_cselect_b32 s1, s5, s4
	s_xor_b32 s1, s1, s3
	s_sub_i32 s1, s1, s3
	s_lshl_b32 s18, s1, 2
